# lean_prio
# speedup vs baseline: 1.0570x; 1.0171x over previous
_Z10lstm_fusedPKfS0_S0_S0_S0_S0_S0_S0_S0_S0_S0_Pf:
	s_load_dwordx16 s[36:51], s[0:1], 0x0
	s_load_dwordx8 s[52:59], s[0:1], 0x40
	s_load_dword s21, s[0:1], 0x60
	v_readfirstlane_b32 s3, v0
	v_and_b32_e32 v69, 63, v0
	v_and_b32_e32 v68, 15, v0
	v_bfe_u32 v1, v0, 4, 2
	s_lshr_b32 s3, s3, 6
	s_lshl_b32 s2, s2, 4
	s_add_i32 s20, s3, s2
	v_lshlrev_b32_e32 v2, 5, v1
	v_mov_b32_e32 v3, 0
	v_lshlrev_b32_e32 v60, 4, v0
	s_lshl_b32 s26, s20, 12
	s_waitcnt lgkmcnt(0)
	s_load_dword s34, s[56:57], 0x0
	v_lshl_add_u64 v[42:43], s[36:37], 0, v[2:3]
	v_lshl_or_b32 v2, v68, 7, s26
	v_lshl_add_u64 v[74:75], v[42:43], 0, v[2:3]
	s_add_u32 s4, s3, 0
	s_mov_b32 s24, 0
	s_mov_b32 s25, 0
	s_sub_u32 s5, s4, 12
	s_mov_b64 s[8:9], s[44:45]
	s_movk_i32 s10, 0x100
	s_movk_i32 s11, 16
	s_movk_i32 s12, 64
	s_mov_b32 s13, 0xbf2562dd
	s_mov_b32 s14, 0xbfa562dd
	s_mov_b32 s15, 1
	s_cmp_lt_u32 s4, 12
	s_cbranch_scc0 .Lpr0_cls
	s_lshl_b32 s5, s4, 1
	s_mov_b64 s[8:9], s[38:39]
	s_movk_i32 s10, 0x80
	s_movk_i32 s11, 32
	s_movk_i32 s12, 16
	s_mov_b32 s13, 0xbfb8aa3b
	s_mov_b32 s14, 0xc038aa3b
.Lpr0_cls:
	s_lshr_b32 s6, s5, 1
	s_and_b32 s7, s5, 1
	s_lshl_b32 s7, s7, 7
	s_mul_i32 s16, s6, 43
	s_lshr_b32 s16, s16, 7
	s_mul_i32 s17, s16, 3
	s_sub_u32 s17, s6, s17
	s_min_u32 s18, s17, 1
	s_add_u32 s18, s18, s17
	s_lshl_b32 s18, s18, 6
	s_lshl_b32 s19, s16, 4
	s_add_u32 s18, s18, s19
	s_lshl_b32 s19, s6, 4
	s_cmp_eq_u32 s15, 1
	s_cselect_b32 s18, s18, s19
	s_cmp_eq_u32 s17, 1
	s_cselect_b32 s19, s14, s13
	s_cmp_eq_u32 s15, 1
	s_cselect_b32 s13, s19, s13
	s_mul_i32 s18, s18, s10
	s_add_u32 s18, s18, s7
	s_add_u32 s22, s8, s12
	s_addc_u32 s23, s9, 0
	v_mul_u32_u24_e32 v57, s10, v68
	v_mad_u32_u24 v57, v1, s11, v57
	v_add_u32_e32 v54, s18, v57
	v_mov_b32_e32 v48, s13
	global_load_dwordx4 v[18:21], v54, s[8:9]
	global_load_dwordx4 v[22:25], v54, s[22:23]
	s_add_u32 s4, s3, 16
	s_mov_b32 s24, 0
	s_mov_b32 s25, 0
	s_sub_u32 s5, s4, 12
	s_mov_b64 s[8:9], s[44:45]
	s_movk_i32 s10, 0x100
	s_movk_i32 s11, 16
	s_movk_i32 s12, 64
	s_mov_b32 s13, 0xbf2562dd
	s_mov_b32 s14, 0xbfa562dd
	s_mov_b32 s15, 1
.Lpr1_cls:
	s_lshr_b32 s6, s5, 1
	s_and_b32 s7, s5, 1
	s_lshl_b32 s7, s7, 7
	s_mul_i32 s16, s6, 43
	s_lshr_b32 s16, s16, 7
	s_mul_i32 s17, s16, 3
	s_sub_u32 s17, s6, s17
	s_min_u32 s18, s17, 1
	s_add_u32 s18, s18, s17
	s_lshl_b32 s18, s18, 6
	s_lshl_b32 s19, s16, 4
	s_add_u32 s18, s18, s19
	s_lshl_b32 s19, s6, 4
	s_cmp_eq_u32 s15, 1
	s_cselect_b32 s18, s18, s19
	s_cmp_eq_u32 s17, 1
	s_cselect_b32 s19, s14, s13
	s_cmp_eq_u32 s15, 1
	s_cselect_b32 s13, s19, s13
	s_mul_i32 s18, s18, s10
	s_add_u32 s18, s18, s7
	s_add_u32 s22, s8, s12
	s_addc_u32 s23, s9, 0
	v_mul_u32_u24_e32 v57, s10, v68
	v_mad_u32_u24 v57, v1, s11, v57
	v_add_u32_e32 v55, s18, v57
	v_mov_b32_e32 v50, s13
	global_load_dwordx4 v[26:29], v55, s[8:9]
	global_load_dwordx4 v[30:33], v55, s[22:23]
	s_add_u32 s4, s3, 32
	s_mov_b32 s24, 0
	s_mov_b32 s25, 0
	s_sub_u32 s5, s4, 12
	s_mov_b64 s[8:9], s[44:45]
	s_movk_i32 s10, 0x100
	s_movk_i32 s11, 16
	s_movk_i32 s12, 64
	s_mov_b32 s13, 0xbf2562dd
	s_mov_b32 s14, 0xbfa562dd
	s_mov_b32 s15, 1
	s_cmp_lt_u32 s4, 36
	s_cbranch_scc1 .Lpr2_cls
	s_mov_b32 s15, 0
	s_sub_u32 s5, s4, 36
	s_mov_b64 s[8:9], s[50:51]
	s_mov_b32 s13, 0x3ee54621
	s_cmp_lt_u32 s4, 40
	s_cbranch_scc1 .Lpr2_cls
	s_mov_b32 s5, 0
	s_mov_b64 s[8:9], s[54:55]
	s_movk_i32 s10, 0
	s_mov_b32 s13, 0xbfb8aa3b
	s_mov_b32 s24, 1
	s_cmp_gt_u32 s4, 40
	s_cselect_b32 s25, 1, 0
.Lpr2_cls:
	s_lshr_b32 s6, s5, 1
	s_and_b32 s7, s5, 1
	s_lshl_b32 s7, s7, 7
	s_mul_i32 s16, s6, 43
	s_lshr_b32 s16, s16, 7
	s_mul_i32 s17, s16, 3
	s_sub_u32 s17, s6, s17
	s_min_u32 s18, s17, 1
	s_add_u32 s18, s18, s17
	s_lshl_b32 s18, s18, 6
	s_lshl_b32 s19, s16, 4
	s_add_u32 s18, s18, s19
	s_lshl_b32 s19, s6, 4
	s_cmp_eq_u32 s15, 1
	s_cselect_b32 s18, s18, s19
	s_cmp_eq_u32 s17, 1
	s_cselect_b32 s19, s14, s13
	s_cmp_eq_u32 s15, 1
	s_cselect_b32 s13, s19, s13
	s_mul_i32 s18, s18, s10
	s_add_u32 s18, s18, s7
	s_add_u32 s22, s8, s12
	s_addc_u32 s23, s9, 0
	v_mul_u32_u24_e32 v57, s10, v68
	v_mad_u32_u24 v57, v1, s11, v57
	v_add_u32_e32 v56, s18, v57
	v_mov_b32_e32 v52, s13
	s_cmp_eq_u32 s24, 1
	s_cbranch_scc0 .Lpr2_nofc2
	v_and_b32_e32 v58, 11, v68
	v_cmp_eq_u32_e32 vcc, 0, v58
	s_nop 1
	v_cndmask_b32_e32 v52, 0, v52, vcc
.Lpr2_nofc2:
	global_load_dwordx4 v[34:37], v56, s[8:9]
	global_load_dwordx4 v[44:47], v56, s[22:23]
	s_cmp_gt_u32 s3, 6
	s_cbranch_scc1 .Lpb_skip
	s_cmp_eq_u32 s3, 6
	s_cbranch_scc1 .Lpb_fc
	s_mov_b64 s[8:9], s[40:41]
	s_mov_b64 s[22:23], s[42:43]
	s_mov_b32 s4, s3
	s_cmp_lt_u32 s3, 3
	s_cbranch_scc1 .Lpb_l1
	s_mov_b64 s[8:9], s[46:47]
	s_mov_b64 s[22:23], s[48:49]
	s_sub_u32 s4, s3, 3
.Lpb_l1:
	s_lshl_b32 s4, s4, 2
	v_add_u32_e32 v57, s4, v1
	v_mul_u32_u24_e32 v58, 43, v57
	v_lshrrev_b32_e32 v58, 7, v58
	v_mad_i32_i24 v59, v58, -3, v57
	v_min_u32_e32 v61, 1, v59
	v_add_u32_e32 v61, v61, v59
	v_lshlrev_b32_e32 v61, 6, v61
	v_lshl_add_u32 v61, v58, 4, v61
	v_add_lshl_u32 v61, v61, v68, 2
	v_cmp_eq_u32_e32 vcc, 1, v59
	v_mov_b32_e32 v62, 0xbfb8aa3b
	v_mov_b32_e32 v63, 0xc038aa3b
	v_cndmask_b32_e32 v76, v62, v63, vcc
	v_mov_b32_e32 v62, 0x41a80000
	v_cndmask_b32_e32 v77, 0, v62, vcc
	global_load_dword v78, v61, s[8:9]
	global_load_dword v79, v61, s[22:23]
	s_branch .Lpb_skip
.Lpb_fc:
	v_and_b32_e32 v61, 31, v69
	v_lshlrev_b32_e32 v61, 2, v61
	v_mov_b32_e32 v76, 0.5
	v_mov_b32_e32 v77, 0
	global_load_dword v78, v61, s[52:53]
	global_load_dword v79, v61, s[52:53]
.Lpb_skip:
	global_load_dwordx4 v[10:13], v[74:75], off offset:16 nt
	global_load_dwordx4 v[14:17], v[74:75], off nt
	global_load_dwordx4 v[2:5], v[74:75], off offset:2064 nt
	global_load_dwordx4 v[6:9], v[74:75], off offset:2048 nt
	s_waitcnt vmcnt(8)
	v_pk_mul_f32 v[18:19], v[18:19], v[48:49] op_sel_hi:[1,0]
	v_pk_mul_f32 v[20:21], v[20:21], v[48:49] op_sel_hi:[1,0]
	v_pk_mul_f32 v[22:23], v[22:23], v[48:49] op_sel_hi:[1,0]
	v_pk_mul_f32 v[24:25], v[24:25], v[48:49] op_sel_hi:[1,0]
	v_cvt_pk_f16_f32 v18, v18, v19
	v_cvt_pk_f16_f32 v19, v20, v21
	v_cvt_pk_f16_f32 v20, v22, v23
	v_cvt_pk_f16_f32 v21, v24, v25
	ds_write_b128 v60, v[18:21]
	s_waitcnt vmcnt(6)
	v_pk_mul_f32 v[26:27], v[26:27], v[50:51] op_sel_hi:[1,0]
	v_pk_mul_f32 v[28:29], v[28:29], v[50:51] op_sel_hi:[1,0]
	v_pk_mul_f32 v[30:31], v[30:31], v[50:51] op_sel_hi:[1,0]
	v_pk_mul_f32 v[32:33], v[32:33], v[50:51] op_sel_hi:[1,0]
	v_cvt_pk_f16_f32 v26, v26, v27
	v_cvt_pk_f16_f32 v27, v28, v29
	v_cvt_pk_f16_f32 v28, v30, v31
	v_cvt_pk_f16_f32 v29, v32, v33
	ds_write_b128 v60, v[26:29] offset:16384
	s_waitcnt vmcnt(4)
	v_pk_mul_f32 v[34:35], v[34:35], v[52:53] op_sel_hi:[1,0]
	v_pk_mul_f32 v[36:37], v[36:37], v[52:53] op_sel_hi:[1,0]
	v_pk_mul_f32 v[44:45], v[44:45], v[52:53] op_sel_hi:[1,0]
	v_pk_mul_f32 v[46:47], v[46:47], v[52:53] op_sel_hi:[1,0]
	v_cvt_pk_f16_f32 v34, v34, v35
	v_cvt_pk_f16_f32 v35, v36, v37
	v_cvt_pk_f16_f32 v36, v44, v45
	v_cvt_pk_f16_f32 v37, v46, v47
	s_cmp_eq_u32 s25, 1
	s_cbranch_scc1 .Lpr2_nowrite
	ds_write_b128 v60, v[34:37] offset:32768
.Lpr2_nowrite:
	s_movk_i32 s4, 0x1a0
	v_cmp_gt_u32_e32 vcc, s4, v0
	v_add_f32_e32 v50, v78, v79
	v_lshlrev_b32_e32 v18, 2, v0
	s_and_saveexec_b64 s[0:1], vcc
	v_fma_f32 v50, v76, v50, -v77
	ds_write_b32 v18, v50 offset:41984
	s_or_b64 exec, exec, s[0:1]
	s_mov_b64 s[14:15], s[58:59]
	s_waitcnt lgkmcnt(0)
	v_mov_b32_e32 v18, 0xbfb8aa3b
	s_lshl_b32 s3, s21, 4
	s_cmpk_gt_i32 s20, 0x7fff
	v_cmp_gt_u32_e32 vcc, 32, v69
	s_waitcnt lgkmcnt(0)
	v_mul_f32_e32 v18, s34, v18
	v_exp_f32_e32 v70, v18
	v_mov_b32_e32 v18, 0
	v_and_b32_e32 v71, 48, v0
	s_mov_b32 s10, s20
	s_barrier
	s_cbranch_scc1 .LBB0_37
	s_sub_i32 s2, s20, s3
	s_add_i32 s9, s3, s20
	s_mov_b32 s4, 1.0
	s_mov_b32 s8, 0x3fb4c4be
	v_lshlrev_b32_e32 v72, 4, v69
	v_cmp_eq_u32_e64 s[0:1], 1, v1
	v_lshl_add_u32 v38, s2, 5, v69
	s_lshl_b32 s7, s21, 9
	v_mov_b32_e32 v18, 0
	s_mov_b32 s12, 0
	s_mov_b32 s2, 0x4a000000
	s_mov_b32 s5, s4
	s_mov_b32 s6, 0x3f34c4be
	v_mov_b64_e32 v[40:41], s[8:9]
	s_mov_b32 s8, 0x400a34e2
	s_mov_b32 s33, 0
	s_branch .LBB0_35

	.amdhsa_kernel _Z10lstm_fusedPKfS0_S0_S0_S0_S0_S0_S0_S0_S0_S0_Pf
		.amdhsa_group_segment_fixed_size 43648
		.amdhsa_private_segment_fixed_size 0
		.amdhsa_kernarg_size 352
		.amdhsa_user_sgpr_count 2
		.amdhsa_user_sgpr_dispatch_ptr 0
		.amdhsa_user_sgpr_queue_ptr 0
		.amdhsa_user_sgpr_kernarg_segment_ptr 1
		.amdhsa_user_sgpr_dispatch_id 0
		.amdhsa_user_sgpr_kernarg_preload_length 0
		.amdhsa_user_sgpr_kernarg_preload_offset 0
		.amdhsa_user_sgpr_private_segment_size 0
		.amdhsa_uses_dynamic_stack 0
		.amdhsa_enable_private_segment 0
		.amdhsa_system_sgpr_workgroup_id_x 1
		.amdhsa_system_sgpr_workgroup_id_y 0
		.amdhsa_system_sgpr_workgroup_id_z 0
		.amdhsa_system_sgpr_workgroup_info 0
		.amdhsa_system_vgpr_workitem_id 0
		.amdhsa_next_free_vgpr 128
		.amdhsa_next_free_sgpr 60
		.amdhsa_accum_offset 128
		.amdhsa_reserve_vcc 1
		.amdhsa_float_round_mode_32 0
		.amdhsa_float_round_mode_16_64 0
		.amdhsa_float_denorm_mode_32 3
		.amdhsa_float_denorm_mode_16_64 3
		.amdhsa_dx10_clamp 1
		.amdhsa_ieee_mode 1
		.amdhsa_fp16_overflow 0
		.amdhsa_tg_split 0
		.amdhsa_exception_fp_ieee_invalid_op 0
		.amdhsa_exception_fp_denorm_src 0
		.amdhsa_exception_fp_ieee_div_zero 0
		.amdhsa_exception_fp_ieee_overflow 0
		.amdhsa_exception_fp_ieee_underflow 0
		.amdhsa_exception_fp_ieee_inexact 0
		.amdhsa_exception_int_div_zero 0
	.end_amdhsa_kernel

amdhsa.kernels:
  - .agpr_count:     0
    .args:
      - .actual_access:  read_only
        .address_space:  global
        .offset:         0
        .size:           8
        .value_kind:     global_buffer
      - .actual_access:  read_only
        .address_space:  global
        .offset:         8
        .size:           8
        .value_kind:     global_buffer
      - .actual_access:  read_only
        .address_space:  global
        .offset:         16
        .size:           8
        .value_kind:     global_buffer
      - .actual_access:  read_only
        .address_space:  global
        .offset:         24
        .size:           8
        .value_kind:     global_buffer
      - .actual_access:  read_only
        .address_space:  global
        .offset:         32
        .size:           8
        .value_kind:     global_buffer
      - .actual_access:  read_only
        .address_space:  global
        .offset:         40
        .size:           8
        .value_kind:     global_buffer
      - .actual_access:  read_only
        .address_space:  global
        .offset:         48
        .size:           8
        .value_kind:     global_buffer
      - .actual_access:  read_only
        .address_space:  global
        .offset:         56
        .size:           8
        .value_kind:     global_buffer
      - .actual_access:  read_only
        .address_space:  global
        .offset:         64
        .size:           8
        .value_kind:     global_buffer
      - .actual_access:  read_only
        .address_space:  global
        .offset:         72
        .size:           8
        .value_kind:     global_buffer
      - .actual_access:  read_only
        .address_space:  global
        .offset:         80
        .size:           8
        .value_kind:     global_buffer
      - .actual_access:  write_only
        .address_space:  global
        .offset:         88
        .size:           8
        .value_kind:     global_buffer
      - .offset:         96
        .size:           4
        .value_kind:     hidden_block_count_x
      - .offset:         100
        .size:           4
        .value_kind:     hidden_block_count_y
      - .offset:         104
        .size:           4
        .value_kind:     hidden_block_count_z
      - .offset:         108
        .size:           2
        .value_kind:     hidden_group_size_x
      - .offset:         110
        .size:           2
        .value_kind:     hidden_group_size_y
      - .offset:         112
        .size:           2
        .value_kind:     hidden_group_size_z
      - .offset:         114
        .size:           2
        .value_kind:     hidden_remainder_x
      - .offset:         116
        .size:           2
        .value_kind:     hidden_remainder_y
      - .offset:         118
        .size:           2
        .value_kind:     hidden_remainder_z
      - .offset:         136
        .size:           8
        .value_kind:     hidden_global_offset_x
      - .offset:         144
        .size:           8
        .value_kind:     hidden_global_offset_y
      - .offset:         152
        .size:           8
        .value_kind:     hidden_global_offset_z
      - .offset:         160
        .size:           2
        .value_kind:     hidden_grid_dims
    .group_segment_fixed_size: 43648
    .kernarg_segment_align: 8
    .kernarg_segment_size: 352
    .language:       OpenCL C
    .language_version:
      - 2
      - 0
    .max_flat_workgroup_size: 1024
    .name:           _Z10lstm_fusedPKfS0_S0_S0_S0_S0_S0_S0_S0_S0_S0_Pf
    .private_segment_fixed_size: 0
    .sgpr_count:     66
    .sgpr_spill_count: 0
    .symbol:         _Z10lstm_fusedPKfS0_S0_S0_S0_S0_S0_S0_S0_S0_S0_Pf.kd
    .uniform_work_group_size: 1
    .uses_dynamic_stack: false
    .vgpr_count:     128
    .vgpr_spill_count: 0
    .wavefront_size: 64
